# PEER weights stage: all 16 partial-sum LDS reads of the 8 tokens issued up front into free VGPRs (one lgkm wait instead of 16 round trips)
# baseline (speedup 1.0000x reference)
; #define GAS __attribute__((address_space(1)))
; #define LAS __attribute__((address_space(3)))
; __device__ __forceinline__ void expert_phase(const Frame& F, int l, int xcc, LAS unsigned char* wl, const LAS unsigned char* zb) {
;     ...
;             unsigned suvq[8][2]; float gtq[8][2];
; #pragma unroll
;             for (int k = 0; k < 8; ++k)
; #pragma unroll
;                 for (int hf = 0; hf < 2; ++hf) { const unsigned e = *(const LAS unsigned short*)(IDL + k * 256 + (hf * 64 + lane) * 2);
;                     suvq[k][hf] = *(const GAS unsigned*)(SUV + e); gtq[k][hf] = *(const GAS float*)(GATE + (size_t)tok(k) * 128 + hf * 64 + lane); }
; #pragma unroll
;             for (int k = 0; k < 8; ++k) {
;                 float wq[2];
; #pragma unroll
;                 for (int hf = 0; hf < 2; ++hf) {
;                     const unsigned suv = suvq[k][hf];
;                     const int kk = hf * 64 + lane;
;                     const float a = (SA[k * 256 + (kk & 7) * 32 + (kk >> 3)] + SA[k * 256 + (kk & 7) * 32 + 16 + (kk >> 3)]) * bf_lo(suv);
;                     wq[hf] = gtq[k][hf] * bf_hi(suv) * 0.5f * a * (1.0f + erff(a * 0.7071067811865476f));
.LBB0_1159:
	s_waitcnt lgkmcnt(0)
	ds_read_u16 v226, v203 offset:10816
	ds_read_u16 v227, v206 offset:10816
	ds_read_u16 v228, v203 offset:11072
	ds_read_u16 v229, v206 offset:11072
	ds_read_u16 v230, v203 offset:11328
	ds_read_u16 v231, v206 offset:11328
	ds_read_u16 v232, v203 offset:11584
	ds_read_u16 v233, v206 offset:11584
	ds_read_u16 v234, v203 offset:11840
	ds_read_u16 v235, v206 offset:11840
	ds_read_u16 v236, v203 offset:12096
	ds_read_u16 v237, v206 offset:12096
	ds_read_u16 v238, v203 offset:12352
	ds_read_u16 v239, v206 offset:12352
	ds_read_u16 v240, v203 offset:12608
	ds_read_u16 v241, v206 offset:12608
	v_lshl_add_u64 v[0:1], v[160:161], 0, s[2:3]
	s_waitcnt vmcnt(21)
	v_lshl_add_u64 v[32:33], v[160:161], 0, s[44:45]
	s_waitcnt lgkmcnt(0)
	v_lshlrev_b32_e32 v2, 2, v226
	global_load_dword v30, v2, s[18:19]
	global_load_dword v31, v[0:1], off
	v_lshlrev_b32_e32 v2, 2, v227
	global_load_dword v12, v2, s[18:19]
	global_load_dword v29, v[0:1], off offset:256
	v_lshl_add_u64 v[0:1], v[160:161], 0, s[86:87]
	v_lshlrev_b32_e32 v2, 2, v228
	global_load_dword v27, v2, s[18:19]
	global_load_dword v28, v[0:1], off
	v_lshlrev_b32_e32 v2, 2, v229
	global_load_dword v25, v2, s[18:19]
	global_load_dword v26, v[0:1], off offset:256
	v_lshl_add_u64 v[0:1], v[160:161], 0, s[68:69]
	v_lshlrev_b32_e32 v2, 2, v230
	global_load_dword v23, v2, s[18:19]
	global_load_dword v24, v[0:1], off
	v_lshlrev_b32_e32 v2, 2, v231
	global_load_dword v21, v2, s[18:19]
	global_load_dword v22, v[0:1], off offset:256
	v_lshl_add_u64 v[0:1], v[160:161], 0, s[80:81]
	v_lshlrev_b32_e32 v2, 2, v232
	global_load_dword v19, v2, s[18:19]
	global_load_dword v20, v[0:1], off
	v_lshlrev_b32_e32 v2, 2, v233
	global_load_dword v17, v2, s[18:19]
	global_load_dword v18, v[0:1], off offset:256
	v_lshl_add_u64 v[0:1], v[160:161], 0, s[8:9]
	v_lshlrev_b32_e32 v2, 2, v234
	global_load_dword v15, v2, s[18:19]
	global_load_dword v16, v[0:1], off
	v_lshlrev_b32_e32 v2, 2, v235
	global_load_dword v13, v2, s[18:19]
	global_load_dword v14, v[0:1], off offset:256
	v_lshl_add_u64 v[0:1], v[160:161], 0, s[66:67]
	v_lshlrev_b32_e32 v2, 2, v236
	global_load_dword v10, v2, s[18:19]
	global_load_dword v11, v[0:1], off
	v_lshlrev_b32_e32 v2, 2, v237
	global_load_dword v8, v2, s[18:19]
	global_load_dword v9, v[0:1], off offset:256
	v_lshl_add_u64 v[0:1], v[160:161], 0, s[30:31]
	v_lshlrev_b32_e32 v2, 2, v238
	global_load_dword v4, v2, s[18:19]
	global_load_dword v5, v[0:1], off
	v_lshlrev_b32_e32 v2, 2, v239
	global_load_dword v2, v2, s[18:19]
	s_nop 0
	global_load_dword v3, v[0:1], off offset:256
	v_lshlrev_b32_e32 v0, 2, v240
	global_load_dword v0, v0, s[18:19]
	s_nop 0
	global_load_dword v1, v[32:33], off
	v_lshlrev_b32_e32 v6, 2, v241
	global_load_dword v6, v6, s[18:19]
	s_nop 0
	global_load_dword v7, v[32:33], off offset:256
	ds_read2_b32 v[44:45], v204 offset1:16
	ds_read2_b32 v[46:47], v205 offset1:16
	v_add_u32_e32 v78, 0x400, v204
	ds_read2_b32 v[48:49], v78 offset1:16
	v_add_u32_e32 v79, 0x400, v205
	ds_read2_b32 v[50:51], v79 offset1:16
	v_add_u32_e32 v76, 0x800, v204
	ds_read2_b32 v[52:53], v76 offset1:16
	v_add_u32_e32 v77, 0x800, v205
	ds_read2_b32 v[54:55], v77 offset1:16
	v_add_u32_e32 v78, 0xc00, v204
	ds_read2_b32 v[56:57], v78 offset1:16
	v_add_u32_e32 v79, 0xc00, v205
	ds_read2_b32 v[58:59], v79 offset1:16
	v_add_u32_e32 v76, 0x1000, v204
	ds_read2_b32 v[60:61], v76 offset1:16
	v_add_u32_e32 v77, 0x1000, v205
	ds_read2_b32 v[62:63], v77 offset1:16
	v_add_u32_e32 v78, 0x1400, v204
	ds_read2_b32 v[64:65], v78 offset1:16
	v_add_u32_e32 v79, 0x1400, v205
	ds_read2_b32 v[66:67], v79 offset1:16
	v_add_u32_e32 v76, 0x1800, v204
	ds_read2_b32 v[68:69], v76 offset1:16
	v_add_u32_e32 v77, 0x1800, v205
	ds_read2_b32 v[70:71], v77 offset1:16
	v_add_u32_e32 v78, 0x1c00, v204
	ds_read2_b32 v[72:73], v78 offset1:16
	v_add_u32_e32 v79, 0x1c00, v205
	ds_read2_b32 v[74:75], v79 offset1:16
	s_waitcnt lgkmcnt(0)
	v_mov_b32_e32 v32, v44
	v_mov_b32_e32 v33, v45
	v_add_f32_e32 v32, v32, v33
	s_waitcnt vmcnt(31)
	v_lshlrev_b32_e32 v33, 16, v30
	v_mul_f32_e32 v32, v32, v33
	v_mul_f32_e32 v33, 0x3f3504f3, v32
	v_cmp_nlt_f32_e64 s[2:3], |v33|, 1.0
	s_and_saveexec_b64 s[4:5], s[2:3]
	s_xor_b64 s[2:3], exec, s[4:5]
	s_mov_b32 s10, 0xbfb8aa3b
	s_mov_b32 s11, 0x378e98ab
	s_mov_b32 s30, 0x3b7cd369
	s_mov_b32 s31, 0xbcc618b2
	s_mov_b32 s33, 0x3dda74e4
	s_mov_b32 s44, 0x3f228afd
	s_mov_b32 s45, 0x3e03c728
	s_mov_b32 s54, 0x42ce8ed0
	s_mov_b32 s55, 0xc2b17218
	s_cbranch_execz .LBB0_1161
	v_fma_f32 v34, |v33|, s11, v224
	v_fma_f32 v34, |v33|, v34, s30
	v_fma_f32 v34, |v33|, v34, s31
	v_fma_f32 v34, |v33|, v34, s33
	v_fma_f32 v34, |v33|, v34, s44
	v_fma_f32 v34, |v33|, v34, s45
	v_fma_f32 v34, |v33|, v34, |v33|
	v_mul_f32_e32 v35, 0xbfb8aa3b, v34
	v_fma_f32 v36, v34, s10, -v35
	v_rndne_f32_e32 v37, v35
	v_fmac_f32_e32 v36, 0xb2a5705f, v34
	v_sub_f32_e32 v35, v35, v37
	v_add_f32_e32 v35, v35, v36
	v_cvt_i32_f32_e32 v36, v37
	v_exp_f32_e32 v35, v35
	v_cmp_nlt_f32_e32 vcc, s54, v34
	v_ldexp_f32 v35, v35, v36
	s_nop 0
	v_cndmask_b32_e32 v35, 0, v35, vcc
	v_cmp_ngt_f32_e32 vcc, s55, v34
	s_nop 1
	v_cndmask_b32_e32 v34, v225, v35, vcc
	v_sub_f32_e32 v34, 1.0, v34
.LBB0_1161:
	s_or_saveexec_b64 s[2:3], s[2:3]
	s_brev_b32 s58, -2
	s_mov_b32 s64, 0xda24260
	s_mov_b32 s65, 0x42280000
	s_mov_b32 s66, 0x10001
	s_xor_b64 exec, exec, s[2:3]
	v_mul_f32_e32 v34, v33, v33
	v_fmamk_f32 v35, v34, 0xba1345e1, v216
	v_fmaak_f32 v35, v34, v35, 0xbcdac9b8
	v_fmaak_f32 v35, v34, v35, 0x3de703be
	v_fmaak_f32 v35, v34, v35, 0xbec09330
	v_fmaak_f32 v34, v34, v35, 0x3e0375d0
	v_fma_f32 v34, |v33|, v34, |v33|
	s_or_b64 exec, exec, s[2:3]
	v_mov_b32_e32 v36, v46
	v_mov_b32_e32 v37, v47
	v_add_f32_e32 v35, v36, v37
	s_waitcnt vmcnt(29)
	v_lshlrev_b32_e32 v36, 16, v12
	v_mul_f32_e32 v35, v35, v36
	v_mul_f32_e32 v36, 0x3f3504f3, v35
	v_cmp_nlt_f32_e64 s[2:3], |v36|, 1.0
	s_and_saveexec_b64 s[4:5], s[2:3]
	s_xor_b64 s[2:3], exec, s[4:5]
	s_cbranch_execz .LBB0_1165
	v_fma_f32 v37, |v36|, s11, v224
	v_fma_f32 v37, |v36|, v37, s30
	v_fma_f32 v37, |v36|, v37, s31
	v_fma_f32 v37, |v36|, v37, s33
	v_fma_f32 v37, |v36|, v37, s44
	v_fma_f32 v37, |v36|, v37, s45
	v_fma_f32 v37, |v36|, v37, |v36|
	v_mul_f32_e32 v38, 0xbfb8aa3b, v37
	v_fma_f32 v39, v37, s10, -v38
	v_rndne_f32_e32 v40, v38
	v_fmac_f32_e32 v39, 0xb2a5705f, v37
	v_sub_f32_e32 v38, v38, v40
	v_add_f32_e32 v38, v38, v39
	v_cvt_i32_f32_e32 v39, v40
	v_exp_f32_e32 v38, v38
	v_cmp_nlt_f32_e32 vcc, s54, v37
	v_ldexp_f32 v38, v38, v39
	s_nop 0
	v_cndmask_b32_e32 v38, 0, v38, vcc
	v_cmp_ngt_f32_e32 vcc, s55, v37
	s_nop 1
	v_cndmask_b32_e32 v37, v225, v38, vcc
	v_sub_f32_e32 v37, 1.0, v37

; __device__ __forceinline__ void expert_phase(const Frame& F, int l, int xcc, LAS unsigned char* wl, const LAS unsigned char* zb) {
;     ...
;                 for (int hf = 0; hf < 2; ++hf) {
;                     const unsigned suv = suvq[k][hf];
;                     const int kk = hf * 64 + lane;
;                     const float a = (SA[k * 256 + (kk & 7) * 32 + (kk >> 3)] + SA[k * 256 + (kk & 7) * 32 + 16 + (kk >> 3)]) * bf_lo(suv);
;                     wq[hf] = gtq[k][hf] * bf_hi(suv) * 0.5f * a * (1.0f + erff(a * 0.7071067811865476f));
.LBB0_1169:
	s_or_b64 exec, exec, s[2:3]
	v_add_u32_e32 v29, 0x400, v204
	v_mov_b32_e32 v30, v48
	v_mov_b32_e32 v31, v49
	v_add_f32_e32 v29, v30, v31
	s_waitcnt vmcnt(27)
	v_lshlrev_b32_e32 v30, 16, v27
	v_mul_f32_e32 v29, v29, v30
	v_mul_f32_e32 v30, 0x3f3504f3, v29
	v_cmp_nlt_f32_e64 s[2:3], |v30|, 1.0
	s_and_saveexec_b64 s[4:5], s[2:3]
	s_xor_b64 s[2:3], exec, s[4:5]
	s_cbranch_execz .LBB0_1171
	v_fma_f32 v31, |v30|, s11, v224
	v_fma_f32 v31, |v30|, v31, s30
	v_fma_f32 v31, |v30|, v31, s31
	v_fma_f32 v31, |v30|, v31, s33
	v_fma_f32 v31, |v30|, v31, s44
	v_fma_f32 v31, |v30|, v31, s45
	v_fma_f32 v31, |v30|, v31, |v30|
	v_mul_f32_e32 v32, 0xbfb8aa3b, v31
	v_fma_f32 v33, v31, s10, -v32
	v_rndne_f32_e32 v34, v32
	v_fmac_f32_e32 v33, 0xb2a5705f, v31
	v_sub_f32_e32 v32, v32, v34
	v_add_f32_e32 v32, v32, v33
	v_cvt_i32_f32_e32 v33, v34
	v_exp_f32_e32 v32, v32
	v_cmp_nlt_f32_e32 vcc, s54, v31
	v_ldexp_f32 v32, v32, v33
	s_nop 0
	v_cndmask_b32_e32 v32, 0, v32, vcc
	v_cmp_ngt_f32_e32 vcc, s55, v31
	s_nop 1
	v_cndmask_b32_e32 v31, v225, v32, vcc
	v_sub_f32_e32 v31, 1.0, v31
.LBB0_1171:
	s_andn2_saveexec_b64 s[2:3], s[2:3]
	v_mul_f32_e32 v31, v30, v30
	v_fmamk_f32 v32, v31, 0xba1345e1, v216
	v_fmaak_f32 v32, v31, v32, 0xbcdac9b8
	v_fmaak_f32 v32, v31, v32, 0x3de703be
	v_fmaak_f32 v32, v31, v32, 0xbec09330
	v_fmaak_f32 v31, v31, v32, 0x3e0375d0
	v_fma_f32 v31, |v30|, v31, |v30|
	s_or_b64 exec, exec, s[2:3]
	v_add_u32_e32 v32, 0x400, v205
	v_mov_b32_e32 v32, v50
	v_mov_b32_e32 v33, v51
	v_add_f32_e32 v32, v32, v33
	s_waitcnt vmcnt(25)
	v_lshlrev_b32_e32 v33, 16, v25
	v_mul_f32_e32 v32, v32, v33
	v_mul_f32_e32 v33, 0x3f3504f3, v32
	v_cmp_nlt_f32_e64 s[2:3], |v33|, 1.0
	s_and_saveexec_b64 s[4:5], s[2:3]
	s_xor_b64 s[2:3], exec, s[4:5]
	s_cbranch_execz .LBB0_1175
	v_fma_f32 v34, |v33|, s11, v224
	v_fma_f32 v34, |v33|, v34, s30
	v_fma_f32 v34, |v33|, v34, s31
	v_fma_f32 v34, |v33|, v34, s33
	v_fma_f32 v34, |v33|, v34, s44
	v_fma_f32 v34, |v33|, v34, s45
	v_fma_f32 v34, |v33|, v34, |v33|
	v_mul_f32_e32 v35, 0xbfb8aa3b, v34
	v_fma_f32 v36, v34, s10, -v35
	v_rndne_f32_e32 v37, v35
	v_fmac_f32_e32 v36, 0xb2a5705f, v34
	v_sub_f32_e32 v35, v35, v37
	v_add_f32_e32 v35, v35, v36
	v_cvt_i32_f32_e32 v36, v37
	v_exp_f32_e32 v35, v35
	v_cmp_nlt_f32_e32 vcc, s54, v34
	v_ldexp_f32 v35, v35, v36
	s_nop 0
	v_cndmask_b32_e32 v35, 0, v35, vcc
	v_cmp_ngt_f32_e32 vcc, s55, v34
	s_nop 1
	v_cndmask_b32_e32 v34, v225, v35, vcc
	v_sub_f32_e32 v34, 1.0, v34

; __device__ __forceinline__ void expert_phase(const Frame& F, int l, int xcc, LAS unsigned char* wl, const LAS unsigned char* zb) {
;     ...
;                 for (int hf = 0; hf < 2; ++hf) {
;                     const unsigned suv = suvq[k][hf];
;                     const int kk = hf * 64 + lane;
;                     const float a = (SA[k * 256 + (kk & 7) * 32 + (kk >> 3)] + SA[k * 256 + (kk & 7) * 32 + 16 + (kk >> 3)]) * bf_lo(suv);
;                     wq[hf] = gtq[k][hf] * bf_hi(suv) * 0.5f * a * (1.0f + erff(a * 0.7071067811865476f));
.LBB0_1179:
	s_or_b64 exec, exec, s[2:3]
	v_add_u32_e32 v25, 0x800, v204
	v_mov_b32_e32 v26, v52
	v_mov_b32_e32 v27, v53
	v_add_f32_e32 v25, v26, v27
	s_waitcnt vmcnt(23)
	v_lshlrev_b32_e32 v26, 16, v23
	v_mul_f32_e32 v25, v25, v26
	v_mul_f32_e32 v26, 0x3f3504f3, v25
	v_cmp_nlt_f32_e64 s[2:3], |v26|, 1.0
	s_and_saveexec_b64 s[4:5], s[2:3]
	s_xor_b64 s[2:3], exec, s[4:5]
	s_cbranch_execz .LBB0_1181
	v_fma_f32 v27, |v26|, s11, v224
	v_fma_f32 v27, |v26|, v27, s30
	v_fma_f32 v27, |v26|, v27, s31
	v_fma_f32 v27, |v26|, v27, s33
	v_fma_f32 v27, |v26|, v27, s44
	v_fma_f32 v27, |v26|, v27, s45
	v_fma_f32 v27, |v26|, v27, |v26|
	v_mul_f32_e32 v28, 0xbfb8aa3b, v27
	v_fma_f32 v29, v27, s10, -v28
	v_rndne_f32_e32 v30, v28
	v_fmac_f32_e32 v29, 0xb2a5705f, v27
	v_sub_f32_e32 v28, v28, v30
	v_add_f32_e32 v28, v28, v29
	v_cvt_i32_f32_e32 v29, v30
	v_exp_f32_e32 v28, v28
	v_cmp_nlt_f32_e32 vcc, s54, v27
	v_ldexp_f32 v28, v28, v29
	s_nop 0
	v_cndmask_b32_e32 v28, 0, v28, vcc
	v_cmp_ngt_f32_e32 vcc, s55, v27
	s_nop 1
	v_cndmask_b32_e32 v27, v225, v28, vcc
	v_sub_f32_e32 v27, 1.0, v27
.LBB0_1181:
	s_andn2_saveexec_b64 s[2:3], s[2:3]
	v_mul_f32_e32 v27, v26, v26
	v_fmamk_f32 v28, v27, 0xba1345e1, v216
	v_fmaak_f32 v28, v27, v28, 0xbcdac9b8
	v_fmaak_f32 v28, v27, v28, 0x3de703be
	v_fmaak_f32 v28, v27, v28, 0xbec09330
	v_fmaak_f32 v27, v27, v28, 0x3e0375d0
	v_fma_f32 v27, |v26|, v27, |v26|
	s_or_b64 exec, exec, s[2:3]
	v_add_u32_e32 v28, 0x800, v205
	v_mov_b32_e32 v28, v54
	v_mov_b32_e32 v29, v55
	v_add_f32_e32 v28, v28, v29
	s_waitcnt vmcnt(21)
	v_lshlrev_b32_e32 v29, 16, v21
	v_mul_f32_e32 v28, v28, v29
	v_mul_f32_e32 v29, 0x3f3504f3, v28
	v_cmp_nlt_f32_e64 s[2:3], |v29|, 1.0
	s_and_saveexec_b64 s[4:5], s[2:3]
	s_xor_b64 s[2:3], exec, s[4:5]
	s_cbranch_execz .LBB0_1185
	v_fma_f32 v30, |v29|, s11, v224
	v_fma_f32 v30, |v29|, v30, s30
	v_fma_f32 v30, |v29|, v30, s31
	v_fma_f32 v30, |v29|, v30, s33
	v_fma_f32 v30, |v29|, v30, s44
	v_fma_f32 v30, |v29|, v30, s45
	v_fma_f32 v30, |v29|, v30, |v29|
	v_mul_f32_e32 v31, 0xbfb8aa3b, v30
	v_fma_f32 v32, v30, s10, -v31
	v_rndne_f32_e32 v33, v31
	v_fmac_f32_e32 v32, 0xb2a5705f, v30
	v_sub_f32_e32 v31, v31, v33
	v_add_f32_e32 v31, v31, v32
	v_cvt_i32_f32_e32 v32, v33
	v_exp_f32_e32 v31, v31
	v_cmp_nlt_f32_e32 vcc, s54, v30
	v_ldexp_f32 v31, v31, v32
	s_nop 0
	v_cndmask_b32_e32 v31, 0, v31, vcc
	v_cmp_ngt_f32_e32 vcc, s55, v30
	s_nop 1
	v_cndmask_b32_e32 v30, v225, v31, vcc
	v_sub_f32_e32 v30, 1.0, v30

; __device__ __forceinline__ void expert_phase(const Frame& F, int l, int xcc, LAS unsigned char* wl, const LAS unsigned char* zb) {
;     ...
;                 for (int hf = 0; hf < 2; ++hf) {
;                     const unsigned suv = suvq[k][hf];
;                     const int kk = hf * 64 + lane;
;                     const float a = (SA[k * 256 + (kk & 7) * 32 + (kk >> 3)] + SA[k * 256 + (kk & 7) * 32 + 16 + (kk >> 3)]) * bf_lo(suv);
;                     wq[hf] = gtq[k][hf] * bf_hi(suv) * 0.5f * a * (1.0f + erff(a * 0.7071067811865476f));
.LBB0_1189:
	s_or_b64 exec, exec, s[2:3]
	v_add_u32_e32 v21, 0xc00, v204
	v_mov_b32_e32 v22, v56
	v_mov_b32_e32 v23, v57
	v_add_f32_e32 v21, v22, v23
	s_waitcnt vmcnt(19)
	v_lshlrev_b32_e32 v22, 16, v19
	v_mul_f32_e32 v21, v21, v22
	v_mul_f32_e32 v22, 0x3f3504f3, v21
	v_cmp_nlt_f32_e64 s[2:3], |v22|, 1.0
	s_and_saveexec_b64 s[4:5], s[2:3]
	s_xor_b64 s[2:3], exec, s[4:5]
	s_cbranch_execz .LBB0_1191
	v_fma_f32 v23, |v22|, s11, v224
	v_fma_f32 v23, |v22|, v23, s30
	v_fma_f32 v23, |v22|, v23, s31
	v_fma_f32 v23, |v22|, v23, s33
	v_fma_f32 v23, |v22|, v23, s44
	v_fma_f32 v23, |v22|, v23, s45
	v_fma_f32 v23, |v22|, v23, |v22|
	v_mul_f32_e32 v24, 0xbfb8aa3b, v23
	v_fma_f32 v25, v23, s10, -v24
	v_rndne_f32_e32 v26, v24
	v_fmac_f32_e32 v25, 0xb2a5705f, v23
	v_sub_f32_e32 v24, v24, v26
	v_add_f32_e32 v24, v24, v25
	v_cvt_i32_f32_e32 v25, v26
	v_exp_f32_e32 v24, v24
	v_cmp_nlt_f32_e32 vcc, s54, v23
	v_ldexp_f32 v24, v24, v25
	s_nop 0
	v_cndmask_b32_e32 v24, 0, v24, vcc
	v_cmp_ngt_f32_e32 vcc, s55, v23
	s_nop 1
	v_cndmask_b32_e32 v23, v225, v24, vcc
	v_sub_f32_e32 v23, 1.0, v23
.LBB0_1191:
	s_andn2_saveexec_b64 s[2:3], s[2:3]
	v_mul_f32_e32 v23, v22, v22
	v_fmamk_f32 v24, v23, 0xba1345e1, v216
	v_fmaak_f32 v24, v23, v24, 0xbcdac9b8
	v_fmaak_f32 v24, v23, v24, 0x3de703be
	v_fmaak_f32 v24, v23, v24, 0xbec09330
	v_fmaak_f32 v23, v23, v24, 0x3e0375d0
	v_fma_f32 v23, |v22|, v23, |v22|
	s_or_b64 exec, exec, s[2:3]
	v_add_u32_e32 v24, 0xc00, v205
	v_mov_b32_e32 v24, v58
	v_mov_b32_e32 v25, v59
	v_add_f32_e32 v24, v24, v25
	s_waitcnt vmcnt(17)
	v_lshlrev_b32_e32 v25, 16, v17
	v_mul_f32_e32 v24, v24, v25
	v_mul_f32_e32 v25, 0x3f3504f3, v24
	v_cmp_nlt_f32_e64 s[2:3], |v25|, 1.0
	s_and_saveexec_b64 s[4:5], s[2:3]
	s_xor_b64 s[2:3], exec, s[4:5]
	s_cbranch_execz .LBB0_1195
	v_fma_f32 v26, |v25|, s11, v224
	v_fma_f32 v26, |v25|, v26, s30
	v_fma_f32 v26, |v25|, v26, s31
	v_fma_f32 v26, |v25|, v26, s33
	v_fma_f32 v26, |v25|, v26, s44
	v_fma_f32 v26, |v25|, v26, s45
	v_fma_f32 v26, |v25|, v26, |v25|
	v_mul_f32_e32 v27, 0xbfb8aa3b, v26
	v_fma_f32 v28, v26, s10, -v27
	v_rndne_f32_e32 v29, v27
	v_fmac_f32_e32 v28, 0xb2a5705f, v26
	v_sub_f32_e32 v27, v27, v29
	v_add_f32_e32 v27, v27, v28
	v_cvt_i32_f32_e32 v28, v29
	v_exp_f32_e32 v27, v27
	v_cmp_nlt_f32_e32 vcc, s54, v26
	v_ldexp_f32 v27, v27, v28
	s_nop 0
	v_cndmask_b32_e32 v27, 0, v27, vcc
	v_cmp_ngt_f32_e32 vcc, s55, v26
	s_nop 1
	v_cndmask_b32_e32 v26, v225, v27, vcc
	v_sub_f32_e32 v26, 1.0, v26

; __device__ __forceinline__ void expert_phase(const Frame& F, int l, int xcc, LAS unsigned char* wl, const LAS unsigned char* zb) {
;     ...
;                 for (int hf = 0; hf < 2; ++hf) {
;                     const unsigned suv = suvq[k][hf];
;                     const int kk = hf * 64 + lane;
;                     const float a = (SA[k * 256 + (kk & 7) * 32 + (kk >> 3)] + SA[k * 256 + (kk & 7) * 32 + 16 + (kk >> 3)]) * bf_lo(suv);
;                     wq[hf] = gtq[k][hf] * bf_hi(suv) * 0.5f * a * (1.0f + erff(a * 0.7071067811865476f));
.LBB0_1199:
	s_or_b64 exec, exec, s[2:3]
	v_add_u32_e32 v17, 0x1000, v204
	v_mov_b32_e32 v18, v60
	v_mov_b32_e32 v19, v61
	v_add_f32_e32 v17, v18, v19
	s_waitcnt vmcnt(15)
	v_lshlrev_b32_e32 v18, 16, v15
	v_mul_f32_e32 v17, v17, v18
	v_mul_f32_e32 v18, 0x3f3504f3, v17
	v_cmp_nlt_f32_e64 s[2:3], |v18|, 1.0
	s_and_saveexec_b64 s[4:5], s[2:3]
	s_xor_b64 s[2:3], exec, s[4:5]
	s_cbranch_execz .LBB0_1201
	v_fma_f32 v19, |v18|, s11, v224
	v_fma_f32 v19, |v18|, v19, s30
	v_fma_f32 v19, |v18|, v19, s31
	v_fma_f32 v19, |v18|, v19, s33
	v_fma_f32 v19, |v18|, v19, s44
	v_fma_f32 v19, |v18|, v19, s45
	v_fma_f32 v19, |v18|, v19, |v18|
	v_mul_f32_e32 v20, 0xbfb8aa3b, v19
	v_fma_f32 v21, v19, s10, -v20
	v_rndne_f32_e32 v22, v20
	v_fmac_f32_e32 v21, 0xb2a5705f, v19
	v_sub_f32_e32 v20, v20, v22
	v_add_f32_e32 v20, v20, v21
	v_cvt_i32_f32_e32 v21, v22
	v_exp_f32_e32 v20, v20
	v_cmp_nlt_f32_e32 vcc, s54, v19
	v_ldexp_f32 v20, v20, v21
	s_nop 0
	v_cndmask_b32_e32 v20, 0, v20, vcc
	v_cmp_ngt_f32_e32 vcc, s55, v19
	s_nop 1
	v_cndmask_b32_e32 v19, v225, v20, vcc
	v_sub_f32_e32 v19, 1.0, v19
.LBB0_1201:
	s_andn2_saveexec_b64 s[2:3], s[2:3]
	v_mul_f32_e32 v19, v18, v18
	v_fmamk_f32 v20, v19, 0xba1345e1, v216
	v_fmaak_f32 v20, v19, v20, 0xbcdac9b8
	v_fmaak_f32 v20, v19, v20, 0x3de703be
	v_fmaak_f32 v20, v19, v20, 0xbec09330
	v_fmaak_f32 v19, v19, v20, 0x3e0375d0
	v_fma_f32 v19, |v18|, v19, |v18|
	s_or_b64 exec, exec, s[2:3]
	v_add_u32_e32 v20, 0x1000, v205
	v_mov_b32_e32 v20, v62
	v_mov_b32_e32 v21, v63
	v_add_f32_e32 v20, v20, v21
	s_waitcnt vmcnt(13)
	v_lshlrev_b32_e32 v21, 16, v13
	v_mul_f32_e32 v20, v20, v21
	v_mul_f32_e32 v21, 0x3f3504f3, v20
	v_cmp_nlt_f32_e64 s[2:3], |v21|, 1.0
	s_and_saveexec_b64 s[4:5], s[2:3]
	s_xor_b64 s[2:3], exec, s[4:5]
	s_cbranch_execz .LBB0_1205
	v_fma_f32 v22, |v21|, s11, v224
	v_fma_f32 v22, |v21|, v22, s30
	v_fma_f32 v22, |v21|, v22, s31
	v_fma_f32 v22, |v21|, v22, s33
	v_fma_f32 v22, |v21|, v22, s44
	v_fma_f32 v22, |v21|, v22, s45
	v_fma_f32 v22, |v21|, v22, |v21|
	v_mul_f32_e32 v23, 0xbfb8aa3b, v22
	v_fma_f32 v24, v22, s10, -v23
	v_rndne_f32_e32 v25, v23
	v_fmac_f32_e32 v24, 0xb2a5705f, v22
	v_sub_f32_e32 v23, v23, v25
	v_add_f32_e32 v23, v23, v24
	v_cvt_i32_f32_e32 v24, v25
	v_exp_f32_e32 v23, v23
	v_cmp_nlt_f32_e32 vcc, s54, v22
	v_ldexp_f32 v23, v23, v24
	s_nop 0
	v_cndmask_b32_e32 v23, 0, v23, vcc
	v_cmp_ngt_f32_e32 vcc, s55, v22
	s_nop 1
	v_cndmask_b32_e32 v22, v225, v23, vcc
	v_sub_f32_e32 v22, 1.0, v22

; __device__ __forceinline__ void expert_phase(const Frame& F, int l, int xcc, LAS unsigned char* wl, const LAS unsigned char* zb) {
;     ...
;                 for (int hf = 0; hf < 2; ++hf) {
;                     const unsigned suv = suvq[k][hf];
;                     const int kk = hf * 64 + lane;
;                     const float a = (SA[k * 256 + (kk & 7) * 32 + (kk >> 3)] + SA[k * 256 + (kk & 7) * 32 + 16 + (kk >> 3)]) * bf_lo(suv);
;                     wq[hf] = gtq[k][hf] * bf_hi(suv) * 0.5f * a * (1.0f + erff(a * 0.7071067811865476f));
.LBB0_1209:
	s_or_b64 exec, exec, s[2:3]
	v_add_u32_e32 v13, 0x1400, v204
	v_mov_b32_e32 v14, v64
	v_mov_b32_e32 v15, v65
	v_add_f32_e32 v13, v14, v15
	s_waitcnt vmcnt(11)
	v_lshlrev_b32_e32 v14, 16, v10
	v_mul_f32_e32 v13, v13, v14
	v_mul_f32_e32 v14, 0x3f3504f3, v13
	v_cmp_nlt_f32_e64 s[2:3], |v14|, 1.0
	s_and_saveexec_b64 s[4:5], s[2:3]
	s_xor_b64 s[2:3], exec, s[4:5]
	s_cbranch_execz .LBB0_1211
	v_fma_f32 v15, |v14|, s11, v224
	v_fma_f32 v15, |v14|, v15, s30
	v_fma_f32 v15, |v14|, v15, s31
	v_fma_f32 v15, |v14|, v15, s33
	v_fma_f32 v15, |v14|, v15, s44
	v_fma_f32 v15, |v14|, v15, s45
	v_fma_f32 v15, |v14|, v15, |v14|
	v_mul_f32_e32 v16, 0xbfb8aa3b, v15
	v_fma_f32 v17, v15, s10, -v16
	v_rndne_f32_e32 v18, v16
	v_fmac_f32_e32 v17, 0xb2a5705f, v15
	v_sub_f32_e32 v16, v16, v18
	v_add_f32_e32 v16, v16, v17
	v_cvt_i32_f32_e32 v17, v18
	v_exp_f32_e32 v16, v16
	v_cmp_nlt_f32_e32 vcc, s54, v15
	v_ldexp_f32 v16, v16, v17
	s_nop 0
	v_cndmask_b32_e32 v16, 0, v16, vcc
	v_cmp_ngt_f32_e32 vcc, s55, v15
	s_nop 1
	v_cndmask_b32_e32 v15, v225, v16, vcc
	v_sub_f32_e32 v15, 1.0, v15
.LBB0_1211:
	s_andn2_saveexec_b64 s[2:3], s[2:3]
	v_mul_f32_e32 v15, v14, v14
	v_fmamk_f32 v16, v15, 0xba1345e1, v216
	v_fmaak_f32 v16, v15, v16, 0xbcdac9b8
	v_fmaak_f32 v16, v15, v16, 0x3de703be
	v_fmaak_f32 v16, v15, v16, 0xbec09330
	v_fmaak_f32 v15, v15, v16, 0x3e0375d0
	v_fma_f32 v15, |v14|, v15, |v14|
	s_or_b64 exec, exec, s[2:3]
	v_add_u32_e32 v16, 0x1400, v205
	v_mov_b32_e32 v16, v66
	v_mov_b32_e32 v17, v67
	v_add_f32_e32 v16, v16, v17
	s_waitcnt vmcnt(9)
	v_lshlrev_b32_e32 v17, 16, v8
	v_mul_f32_e32 v16, v16, v17
	v_mul_f32_e32 v17, 0x3f3504f3, v16
	v_cmp_nlt_f32_e64 s[2:3], |v17|, 1.0
	s_and_saveexec_b64 s[4:5], s[2:3]
	s_xor_b64 s[2:3], exec, s[4:5]
	s_cbranch_execz .LBB0_1215
	v_fma_f32 v18, |v17|, s11, v224
	v_fma_f32 v18, |v17|, v18, s30
	v_fma_f32 v18, |v17|, v18, s31
	v_fma_f32 v18, |v17|, v18, s33
	v_fma_f32 v18, |v17|, v18, s44
	v_fma_f32 v18, |v17|, v18, s45
	v_fma_f32 v18, |v17|, v18, |v17|
	v_mul_f32_e32 v19, 0xbfb8aa3b, v18
	v_fma_f32 v20, v18, s10, -v19
	v_rndne_f32_e32 v21, v19
	v_fmac_f32_e32 v20, 0xb2a5705f, v18
	v_sub_f32_e32 v19, v19, v21
	v_add_f32_e32 v19, v19, v20
	v_cvt_i32_f32_e32 v20, v21
	v_exp_f32_e32 v19, v19
	v_cmp_nlt_f32_e32 vcc, s54, v18
	v_ldexp_f32 v19, v19, v20
	s_nop 0
	v_cndmask_b32_e32 v19, 0, v19, vcc
	v_cmp_ngt_f32_e32 vcc, s55, v18
	s_nop 1
	v_cndmask_b32_e32 v18, v225, v19, vcc
	v_sub_f32_e32 v18, 1.0, v18

; __device__ __forceinline__ void expert_phase(const Frame& F, int l, int xcc, LAS unsigned char* wl, const LAS unsigned char* zb) {
;     ...
;                 for (int hf = 0; hf < 2; ++hf) {
;                     const unsigned suv = suvq[k][hf];
;                     const int kk = hf * 64 + lane;
;                     const float a = (SA[k * 256 + (kk & 7) * 32 + (kk >> 3)] + SA[k * 256 + (kk & 7) * 32 + 16 + (kk >> 3)]) * bf_lo(suv);
;                     wq[hf] = gtq[k][hf] * bf_hi(suv) * 0.5f * a * (1.0f + erff(a * 0.7071067811865476f));
.LBB0_1219:
	s_or_b64 exec, exec, s[2:3]
	v_add_u32_e32 v8, 0x1800, v204
	v_mov_b32_e32 v8, v68
	v_mov_b32_e32 v9, v69
	v_add_f32_e32 v8, v8, v9
	s_waitcnt vmcnt(7)
	v_lshlrev_b32_e32 v9, 16, v4
	v_mul_f32_e32 v8, v8, v9
	v_mul_f32_e32 v9, 0x3f3504f3, v8
	v_cmp_nlt_f32_e64 s[2:3], |v9|, 1.0
	s_and_saveexec_b64 s[4:5], s[2:3]
	s_xor_b64 s[2:3], exec, s[4:5]
	s_cbranch_execz .LBB0_1221
	v_fma_f32 v10, |v9|, s11, v224
	v_fma_f32 v10, |v9|, v10, s30
	v_fma_f32 v10, |v9|, v10, s31
	v_fma_f32 v10, |v9|, v10, s33
	v_fma_f32 v10, |v9|, v10, s44
	v_fma_f32 v10, |v9|, v10, s45
	v_fma_f32 v10, |v9|, v10, |v9|
	v_mul_f32_e32 v11, 0xbfb8aa3b, v10
	v_fma_f32 v13, v10, s10, -v11
	v_rndne_f32_e32 v14, v11
	v_fmac_f32_e32 v13, 0xb2a5705f, v10
	v_sub_f32_e32 v11, v11, v14
	v_add_f32_e32 v11, v11, v13
	v_cvt_i32_f32_e32 v13, v14
	v_exp_f32_e32 v11, v11
	v_cmp_nlt_f32_e32 vcc, s54, v10
	v_ldexp_f32 v11, v11, v13
	s_nop 0
	v_cndmask_b32_e32 v11, 0, v11, vcc
	v_cmp_ngt_f32_e32 vcc, s55, v10
	s_nop 1
	v_cndmask_b32_e32 v10, v225, v11, vcc
	v_sub_f32_e32 v10, 1.0, v10
.LBB0_1221:
	s_andn2_saveexec_b64 s[2:3], s[2:3]
	v_mul_f32_e32 v10, v9, v9
	v_fmamk_f32 v11, v10, 0xba1345e1, v216
	v_fmaak_f32 v11, v10, v11, 0xbcdac9b8
	v_fmaak_f32 v11, v10, v11, 0x3de703be
	v_fmaak_f32 v11, v10, v11, 0xbec09330
	v_fmaak_f32 v10, v10, v11, 0x3e0375d0
	v_fma_f32 v10, |v9|, v10, |v9|
	s_or_b64 exec, exec, s[2:3]
	v_add_u32_e32 v11, 0x1800, v205
	v_mov_b32_e32 v14, v70
	v_mov_b32_e32 v15, v71
	s_waitcnt vmcnt(5)
	v_lshlrev_b32_e32 v13, 16, v2
	v_add_f32_e32 v11, v14, v15
	v_mul_f32_e32 v11, v11, v13
	v_mul_f32_e32 v13, 0x3f3504f3, v11
	v_cmp_nlt_f32_e64 s[2:3], |v13|, 1.0
	s_and_saveexec_b64 s[4:5], s[2:3]
	s_xor_b64 s[2:3], exec, s[4:5]
	s_cbranch_execz .LBB0_1225
	v_fma_f32 v14, |v13|, s11, v224
	v_fma_f32 v14, |v13|, v14, s30
	v_fma_f32 v14, |v13|, v14, s31
	v_fma_f32 v14, |v13|, v14, s33
	v_fma_f32 v14, |v13|, v14, s44
	v_fma_f32 v14, |v13|, v14, s45
	v_fma_f32 v14, |v13|, v14, |v13|
	v_mul_f32_e32 v15, 0xbfb8aa3b, v14
	v_fma_f32 v16, v14, s10, -v15
	v_rndne_f32_e32 v17, v15
	v_fmac_f32_e32 v16, 0xb2a5705f, v14
	v_sub_f32_e32 v15, v15, v17
	v_add_f32_e32 v15, v15, v16
	v_cvt_i32_f32_e32 v16, v17
	v_exp_f32_e32 v15, v15
	v_cmp_nlt_f32_e32 vcc, s54, v14
	v_ldexp_f32 v15, v15, v16
	s_nop 0
	v_cndmask_b32_e32 v15, 0, v15, vcc
	v_cmp_ngt_f32_e32 vcc, s55, v14
	s_nop 1
	v_cndmask_b32_e32 v14, v225, v15, vcc
	v_sub_f32_e32 v14, 1.0, v14

; __device__ __forceinline__ void expert_phase(const Frame& F, int l, int xcc, LAS unsigned char* wl, const LAS unsigned char* zb) {
;     ...
;                 for (int hf = 0; hf < 2; ++hf) {
;                     const unsigned suv = suvq[k][hf];
;                     const int kk = hf * 64 + lane;
;                     const float a = (SA[k * 256 + (kk & 7) * 32 + (kk >> 3)] + SA[k * 256 + (kk & 7) * 32 + 16 + (kk >> 3)]) * bf_lo(suv);
;                     wq[hf] = gtq[k][hf] * bf_hi(suv) * 0.5f * a * (1.0f + erff(a * 0.7071067811865476f));
.LBB0_1229:
	s_or_b64 exec, exec, s[2:3]
	v_add_u32_e32 v2, 0x1c00, v204
	v_mov_b32_e32 v2, v72
	v_mov_b32_e32 v3, v73
	v_add_f32_e32 v2, v2, v3
	s_waitcnt vmcnt(3)
	v_lshlrev_b32_e32 v3, 16, v0
	v_mul_f32_e32 v2, v2, v3
	v_mul_f32_e32 v3, 0x3f3504f3, v2
	v_cmp_nlt_f32_e64 s[2:3], |v3|, 1.0
	s_and_saveexec_b64 s[4:5], s[2:3]
	s_xor_b64 s[2:3], exec, s[4:5]
	s_cbranch_execz .LBB0_1231
	v_fma_f32 v4, |v3|, s11, v224
	v_fma_f32 v4, |v3|, v4, s30
	v_fma_f32 v4, |v3|, v4, s31
	v_fma_f32 v4, |v3|, v4, s33
	v_fma_f32 v4, |v3|, v4, s44
	v_fma_f32 v4, |v3|, v4, s45
	v_fma_f32 v4, |v3|, v4, |v3|
	v_mul_f32_e32 v5, 0xbfb8aa3b, v4
	v_fma_f32 v8, v4, s10, -v5
	v_rndne_f32_e32 v9, v5
	v_fmac_f32_e32 v8, 0xb2a5705f, v4
	v_sub_f32_e32 v5, v5, v9
	v_add_f32_e32 v5, v5, v8
	v_cvt_i32_f32_e32 v8, v9
	v_exp_f32_e32 v5, v5
	v_cmp_nlt_f32_e32 vcc, s54, v4
	v_ldexp_f32 v5, v5, v8
	s_nop 0
	v_cndmask_b32_e32 v5, 0, v5, vcc
	v_cmp_ngt_f32_e32 vcc, s55, v4
	s_nop 1
	v_cndmask_b32_e32 v4, v225, v5, vcc
	v_sub_f32_e32 v4, 1.0, v4
.LBB0_1231:
	s_andn2_saveexec_b64 s[2:3], s[2:3]
	v_mul_f32_e32 v4, v3, v3
	v_fmamk_f32 v5, v4, 0xba1345e1, v216
	v_fmaak_f32 v5, v4, v5, 0xbcdac9b8
	v_fmaak_f32 v5, v4, v5, 0x3de703be
	v_fmaak_f32 v5, v4, v5, 0xbec09330
	v_fmaak_f32 v4, v4, v5, 0x3e0375d0
	v_fma_f32 v4, |v3|, v4, |v3|
	s_or_b64 exec, exec, s[2:3]
	v_add_u32_e32 v5, 0x1c00, v205
	v_mov_b32_e32 v8, v74
	v_mov_b32_e32 v9, v75
	v_add_f32_e32 v5, v8, v9
	s_waitcnt vmcnt(1)
	v_lshlrev_b32_e32 v8, 16, v6
	v_mul_f32_e32 v8, v5, v8
	v_mul_f32_e32 v5, 0x3f3504f3, v8
	v_cmp_nlt_f32_e64 s[2:3], |v5|, 1.0
	s_and_saveexec_b64 s[4:5], s[2:3]
	s_xor_b64 s[2:3], exec, s[4:5]
	s_cbranch_execz .LBB0_1235
	v_fma_f32 v9, |v5|, s11, v224
	v_fma_f32 v9, |v5|, v9, s30
	v_fma_f32 v9, |v5|, v9, s31
	v_fma_f32 v9, |v5|, v9, s33
	v_fma_f32 v9, |v5|, v9, s44
	v_fma_f32 v9, |v5|, v9, s45
	v_fma_f32 v9, |v5|, v9, |v5|
	v_mul_f32_e32 v10, 0xbfb8aa3b, v9
	v_fma_f32 v11, v9, s10, -v10
	v_rndne_f32_e32 v13, v10
	v_fmac_f32_e32 v11, 0xb2a5705f, v9
	v_sub_f32_e32 v10, v10, v13
	v_add_f32_e32 v10, v10, v11
	v_cvt_i32_f32_e32 v11, v13
	v_exp_f32_e32 v10, v10
	v_cmp_nlt_f32_e32 vcc, s54, v9
	v_ldexp_f32 v10, v10, v11
	s_nop 0
	v_cndmask_b32_e32 v10, 0, v10, vcc
	v_cmp_ngt_f32_e32 vcc, s55, v9
	s_nop 1
	v_cndmask_b32_e32 v9, v225, v10, vcc
	v_sub_f32_e32 v9, 1.0, v9
